# speedup vs baseline: 1.0223x; 1.0223x over previous
.Lno_anc:
	s_or_b64 exec, exec, s[8:9]
	v_mov_b32_e32 v7, 0x80
	s_waitcnt vmcnt(0)
	s_sub_u32 s26, 0xff, s2
	s_mul_i32 s26, s26, 0
	s_lshr_b32 s26, s26, 7
	s_min_u32 s26, s26, 64
	s_cmp_eq_u32 s26, 0
	s_cbranch_scc1 .Lhold_done
